# combine_norm: YE loads of all selected experts issued before one wait (both instances)
# speedup vs baseline: 1.0116x; 1.0018x over previous
.LBB0_1522:
	v_lshl_add_u64 v[26:27], s[48:49], 0, v[24:25]
	v_add_co_u32_e32 v28, vcc, 0x800000, v26
	v_lshl_add_u64 v[30:31], s[48:49], 0, v[22:23]
	global_load_dword v50, v[30:31], off
	v_addc_co_u32_e32 v29, vcc, 0, v27, vcc
	global_load_dwordx2 v[30:31], v[28:29], off
	global_load_dwordx2 v[32:33], v[28:29], off offset:512
	global_load_dwordx2 v[52:53], v[28:29], off offset:1024
	s_nop 0
	global_load_dwordx2 v[28:29], v[28:29], off offset:1536
	s_waitcnt vmcnt(0)
	v_readlane_b32 s4, v50, 0
	s_cmp_lt_i32 s4, 0
	s_cbranch_scc1 .Lcna_0
	s_lshl_b64 s[24:25], s[4:5], 11
	v_lshl_add_u64 v[200:201], v[20:21], 0, s[24:25]
	global_load_dwordx2 v[72:73], v[200:201], off
	global_load_dwordx2 v[74:75], v[200:201], off offset:512
	global_load_dwordx2 v[76:77], v[200:201], off offset:1024
	global_load_dwordx2 v[78:79], v[200:201], off offset:1536
.Lcna_0:
	v_readlane_b32 s4, v50, 1
	s_cmp_lt_i32 s4, 0
	s_cbranch_scc1 .Lcna_1
	s_lshl_b64 s[24:25], s[4:5], 11
	v_lshl_add_u64 v[200:201], v[20:21], 0, s[24:25]
	global_load_dwordx2 v[80:81], v[200:201], off
	global_load_dwordx2 v[82:83], v[200:201], off offset:512
	global_load_dwordx2 v[84:85], v[200:201], off offset:1024
	global_load_dwordx2 v[86:87], v[200:201], off offset:1536
.Lcna_1:
	v_readlane_b32 s4, v50, 2
	s_cmp_lt_i32 s4, 0
	s_cbranch_scc1 .Lcna_2
	s_lshl_b64 s[24:25], s[4:5], 11
	v_lshl_add_u64 v[200:201], v[20:21], 0, s[24:25]
	global_load_dwordx2 v[88:89], v[200:201], off
	global_load_dwordx2 v[90:91], v[200:201], off offset:512
	global_load_dwordx2 v[92:93], v[200:201], off offset:1024
	global_load_dwordx2 v[94:95], v[200:201], off offset:1536
.Lcna_2:
	v_readlane_b32 s4, v50, 3
	s_cmp_lt_i32 s4, 0
	s_cbranch_scc1 .Lcna_3
	s_lshl_b64 s[24:25], s[4:5], 11
	v_lshl_add_u64 v[200:201], v[20:21], 0, s[24:25]
	global_load_dwordx2 v[96:97], v[200:201], off
	global_load_dwordx2 v[98:99], v[200:201], off offset:512
	global_load_dwordx2 v[100:101], v[200:201], off offset:1024
	global_load_dwordx2 v[102:103], v[200:201], off offset:1536
.Lcna_3:
	v_readlane_b32 s4, v50, 4
	s_cmp_lt_i32 s4, 0
	s_cbranch_scc1 .Lcna_4
	s_lshl_b64 s[24:25], s[4:5], 11
	v_lshl_add_u64 v[200:201], v[20:21], 0, s[24:25]
	global_load_dwordx2 v[104:105], v[200:201], off
	global_load_dwordx2 v[106:107], v[200:201], off offset:512
	global_load_dwordx2 v[108:109], v[200:201], off offset:1024
	global_load_dwordx2 v[110:111], v[200:201], off offset:1536
.Lcna_4:
	v_readlane_b32 s4, v50, 5
	s_cmp_lt_i32 s4, 0
	s_cbranch_scc1 .Lcna_5
	s_lshl_b64 s[24:25], s[4:5], 11
	v_lshl_add_u64 v[200:201], v[20:21], 0, s[24:25]
	global_load_dwordx2 v[112:113], v[200:201], off
	global_load_dwordx2 v[114:115], v[200:201], off offset:512
	global_load_dwordx2 v[116:117], v[200:201], off offset:1024
	global_load_dwordx2 v[118:119], v[200:201], off offset:1536
.Lcna_5:
	v_readlane_b32 s4, v50, 6
	s_cmp_lt_i32 s4, 0
	s_cbranch_scc1 .Lcna_6
	s_lshl_b64 s[24:25], s[4:5], 11
	v_lshl_add_u64 v[200:201], v[20:21], 0, s[24:25]
	global_load_dwordx2 v[120:121], v[200:201], off
	global_load_dwordx2 v[122:123], v[200:201], off offset:512
	global_load_dwordx2 v[124:125], v[200:201], off offset:1024
	global_load_dwordx2 v[126:127], v[200:201], off offset:1536
.Lcna_6:
	v_readlane_b32 s4, v50, 7
	s_cmp_lt_i32 s4, 0
	s_cbranch_scc1 .Lcna_7
	s_lshl_b64 s[24:25], s[4:5], 11
	v_lshl_add_u64 v[200:201], v[20:21], 0, s[24:25]
	global_load_dwordx2 v[128:129], v[200:201], off
	global_load_dwordx2 v[130:131], v[200:201], off offset:512
	global_load_dwordx2 v[132:133], v[200:201], off offset:1024
	global_load_dwordx2 v[134:135], v[200:201], off offset:1536
.Lcna_7:
	v_readlane_b32 s4, v50, 8
	s_cmp_lt_i32 s4, 0
	s_cbranch_scc1 .Lcna_8
	s_lshl_b64 s[24:25], s[4:5], 11
	v_lshl_add_u64 v[200:201], v[20:21], 0, s[24:25]
	global_load_dwordx2 v[136:137], v[200:201], off
	global_load_dwordx2 v[138:139], v[200:201], off offset:512
	global_load_dwordx2 v[140:141], v[200:201], off offset:1024
	global_load_dwordx2 v[142:143], v[200:201], off offset:1536
.Lcna_8:
	v_readlane_b32 s4, v50, 9
	s_cmp_lt_i32 s4, 0
	s_cbranch_scc1 .Lcna_9
	s_lshl_b64 s[24:25], s[4:5], 11
	v_lshl_add_u64 v[200:201], v[20:21], 0, s[24:25]
	global_load_dwordx2 v[144:145], v[200:201], off
	global_load_dwordx2 v[146:147], v[200:201], off offset:512
	global_load_dwordx2 v[148:149], v[200:201], off offset:1024
	global_load_dwordx2 v[150:151], v[200:201], off offset:1536
.Lcna_9:
	v_readlane_b32 s4, v50, 10
	s_cmp_lt_i32 s4, 0
	s_cbranch_scc1 .Lcna_10
	s_lshl_b64 s[24:25], s[4:5], 11
	v_lshl_add_u64 v[200:201], v[20:21], 0, s[24:25]
	global_load_dwordx2 v[152:153], v[200:201], off
	global_load_dwordx2 v[154:155], v[200:201], off offset:512
	global_load_dwordx2 v[156:157], v[200:201], off offset:1024
	global_load_dwordx2 v[158:159], v[200:201], off offset:1536
.Lcna_10:
	v_readlane_b32 s4, v50, 11
	s_cmp_lt_i32 s4, 0
	s_cbranch_scc1 .Lcna_11
	s_lshl_b64 s[24:25], s[4:5], 11
	v_lshl_add_u64 v[200:201], v[20:21], 0, s[24:25]
	global_load_dwordx2 v[160:161], v[200:201], off
	global_load_dwordx2 v[162:163], v[200:201], off offset:512
	global_load_dwordx2 v[164:165], v[200:201], off offset:1024
	global_load_dwordx2 v[166:167], v[200:201], off offset:1536
.Lcna_11:
	v_readlane_b32 s4, v50, 12
	s_cmp_lt_i32 s4, 0
	s_cbranch_scc1 .Lcna_12
	s_lshl_b64 s[24:25], s[4:5], 11
	v_lshl_add_u64 v[200:201], v[20:21], 0, s[24:25]
	global_load_dwordx2 v[168:169], v[200:201], off
	global_load_dwordx2 v[170:171], v[200:201], off offset:512
	global_load_dwordx2 v[172:173], v[200:201], off offset:1024
	global_load_dwordx2 v[174:175], v[200:201], off offset:1536
.Lcna_12:
	v_readlane_b32 s4, v50, 13
	s_cmp_lt_i32 s4, 0
	s_cbranch_scc1 .Lcna_13
	s_lshl_b64 s[24:25], s[4:5], 11
	v_lshl_add_u64 v[200:201], v[20:21], 0, s[24:25]
	global_load_dwordx2 v[176:177], v[200:201], off
	global_load_dwordx2 v[178:179], v[200:201], off offset:512
	global_load_dwordx2 v[180:181], v[200:201], off offset:1024
	global_load_dwordx2 v[182:183], v[200:201], off offset:1536
.Lcna_13:
	v_readlane_b32 s4, v50, 14
	s_cmp_lt_i32 s4, 0
	s_cbranch_scc1 .Lcna_14
	s_lshl_b64 s[24:25], s[4:5], 11
	v_lshl_add_u64 v[200:201], v[20:21], 0, s[24:25]
	global_load_dwordx2 v[184:185], v[200:201], off
	global_load_dwordx2 v[186:187], v[200:201], off offset:512
	global_load_dwordx2 v[188:189], v[200:201], off offset:1024
	global_load_dwordx2 v[190:191], v[200:201], off offset:1536
.Lcna_14:
	v_readlane_b32 s4, v50, 15
	s_cmp_lt_i32 s4, 0
	s_cbranch_scc1 .Lcna_15
	s_lshl_b64 s[24:25], s[4:5], 11
	v_lshl_add_u64 v[200:201], v[20:21], 0, s[24:25]
	global_load_dwordx2 v[192:193], v[200:201], off
	global_load_dwordx2 v[194:195], v[200:201], off offset:512
	global_load_dwordx2 v[196:197], v[200:201], off offset:1024
	global_load_dwordx2 v[198:199], v[200:201], off offset:1536
.Lcna_15:
	v_readlane_b32 s4, v50, 0
	s_cmp_lt_i32 s4, 0
	s_waitcnt vmcnt(0)
	v_and_b32_e32 v42, 0xffff0000, v30
	v_readlane_b32 s4, v50, 0
	s_cmp_lt_i32 s4, 0
	v_lshlrev_b32_e32 v43, 16, v30
	v_and_b32_e32 v40, 0xffff0000, v31
	v_lshlrev_b32_e32 v41, 16, v31
	v_and_b32_e32 v38, 0xffff0000, v32
	v_lshlrev_b32_e32 v39, 16, v32
	v_and_b32_e32 v36, 0xffff0000, v33
	v_lshlrev_b32_e32 v37, 16, v33
	v_and_b32_e32 v34, 0xffff0000, v52
	v_lshlrev_b32_e32 v35, 16, v52
	v_and_b32_e32 v32, 0xffff0000, v53
	v_lshlrev_b32_e32 v33, 16, v53
	v_and_b32_e32 v30, 0xffff0000, v28
	v_lshlrev_b32_e32 v31, 16, v28
	v_and_b32_e32 v28, 0xffff0000, v29
	v_lshlrev_b32_e32 v29, 16, v29
	s_cbranch_scc1 .LBB0_1524
	v_and_b32_e32 v60, 0xffff0000, v72
	v_lshlrev_b32_e32 v61, 16, v72
	v_and_b32_e32 v54, 0xffff0000, v73
	v_lshlrev_b32_e32 v55, 16, v73
	v_and_b32_e32 v62, 0xffff0000, v74
	v_lshlrev_b32_e32 v63, 16, v74
	v_and_b32_e32 v56, 0xffff0000, v75
	v_lshlrev_b32_e32 v57, 16, v75
	v_and_b32_e32 v64, 0xffff0000, v76
	v_lshlrev_b32_e32 v65, 16, v76
	v_and_b32_e32 v58, 0xffff0000, v77
	v_lshlrev_b32_e32 v59, 16, v77
	v_and_b32_e32 v66, 0xffff0000, v78
	v_lshlrev_b32_e32 v67, 16, v78
	v_and_b32_e32 v52, 0xffff0000, v79
	v_lshlrev_b32_e32 v53, 16, v79
	v_pk_add_f32 v[42:43], v[42:43], v[60:61]
	v_pk_add_f32 v[40:41], v[40:41], v[54:55]
	v_pk_add_f32 v[38:39], v[38:39], v[62:63]
	v_pk_add_f32 v[36:37], v[36:37], v[56:57]
	v_pk_add_f32 v[34:35], v[34:35], v[64:65]
	v_pk_add_f32 v[32:33], v[32:33], v[58:59]
	v_pk_add_f32 v[30:31], v[30:31], v[66:67]
	v_pk_add_f32 v[28:29], v[28:29], v[52:53]
.LBB0_1524:
	v_readlane_b32 s4, v50, 1
	s_cmp_lt_i32 s4, 0
	s_cbranch_scc1 .LBB0_1526
	v_and_b32_e32 v60, 0xffff0000, v80
	v_lshlrev_b32_e32 v61, 16, v80
	v_and_b32_e32 v54, 0xffff0000, v81
	v_lshlrev_b32_e32 v55, 16, v81
	v_and_b32_e32 v62, 0xffff0000, v82
	v_lshlrev_b32_e32 v63, 16, v82
	v_and_b32_e32 v56, 0xffff0000, v83
	v_lshlrev_b32_e32 v57, 16, v83
	v_and_b32_e32 v64, 0xffff0000, v84
	v_lshlrev_b32_e32 v65, 16, v84
	v_and_b32_e32 v58, 0xffff0000, v85
	v_lshlrev_b32_e32 v59, 16, v85
	v_and_b32_e32 v66, 0xffff0000, v86
	v_lshlrev_b32_e32 v67, 16, v86
	v_and_b32_e32 v52, 0xffff0000, v87
	v_lshlrev_b32_e32 v53, 16, v87
	v_pk_add_f32 v[42:43], v[42:43], v[60:61]
	v_pk_add_f32 v[40:41], v[40:41], v[54:55]
	v_pk_add_f32 v[38:39], v[38:39], v[62:63]
	v_pk_add_f32 v[36:37], v[36:37], v[56:57]
	v_pk_add_f32 v[34:35], v[34:35], v[64:65]
	v_pk_add_f32 v[32:33], v[32:33], v[58:59]
	v_pk_add_f32 v[30:31], v[30:31], v[66:67]
	v_pk_add_f32 v[28:29], v[28:29], v[52:53]
.LBB0_1526:
	v_readlane_b32 s4, v50, 2
	s_cmp_lt_i32 s4, 0
	s_cbranch_scc1 .LBB0_1528
	v_and_b32_e32 v60, 0xffff0000, v88
	v_lshlrev_b32_e32 v61, 16, v88
	v_and_b32_e32 v54, 0xffff0000, v89
	v_lshlrev_b32_e32 v55, 16, v89
	v_and_b32_e32 v62, 0xffff0000, v90
	v_lshlrev_b32_e32 v63, 16, v90
	v_and_b32_e32 v56, 0xffff0000, v91
	v_lshlrev_b32_e32 v57, 16, v91
	v_and_b32_e32 v64, 0xffff0000, v92
	v_lshlrev_b32_e32 v65, 16, v92
	v_and_b32_e32 v58, 0xffff0000, v93
	v_lshlrev_b32_e32 v59, 16, v93
	v_and_b32_e32 v66, 0xffff0000, v94
	v_lshlrev_b32_e32 v67, 16, v94
	v_and_b32_e32 v52, 0xffff0000, v95
	v_lshlrev_b32_e32 v53, 16, v95
	v_pk_add_f32 v[42:43], v[42:43], v[60:61]
	v_pk_add_f32 v[40:41], v[40:41], v[54:55]
	v_pk_add_f32 v[38:39], v[38:39], v[62:63]
	v_pk_add_f32 v[36:37], v[36:37], v[56:57]
	v_pk_add_f32 v[34:35], v[34:35], v[64:65]
	v_pk_add_f32 v[32:33], v[32:33], v[58:59]
	v_pk_add_f32 v[30:31], v[30:31], v[66:67]
	v_pk_add_f32 v[28:29], v[28:29], v[52:53]
.LBB0_1528:
	v_readlane_b32 s4, v50, 3
	s_cmp_lt_i32 s4, 0
	s_cbranch_scc1 .LBB0_1530
	v_and_b32_e32 v60, 0xffff0000, v96
	v_lshlrev_b32_e32 v61, 16, v96
	v_and_b32_e32 v54, 0xffff0000, v97
	v_lshlrev_b32_e32 v55, 16, v97
	v_and_b32_e32 v62, 0xffff0000, v98
	v_lshlrev_b32_e32 v63, 16, v98
	v_and_b32_e32 v56, 0xffff0000, v99
	v_lshlrev_b32_e32 v57, 16, v99
	v_and_b32_e32 v64, 0xffff0000, v100
	v_lshlrev_b32_e32 v65, 16, v100
	v_and_b32_e32 v58, 0xffff0000, v101
	v_lshlrev_b32_e32 v59, 16, v101
	v_and_b32_e32 v66, 0xffff0000, v102
	v_lshlrev_b32_e32 v67, 16, v102
	v_and_b32_e32 v52, 0xffff0000, v103
	v_lshlrev_b32_e32 v53, 16, v103
	v_pk_add_f32 v[42:43], v[42:43], v[60:61]
	v_pk_add_f32 v[40:41], v[40:41], v[54:55]
	v_pk_add_f32 v[38:39], v[38:39], v[62:63]
	v_pk_add_f32 v[36:37], v[36:37], v[56:57]
	v_pk_add_f32 v[34:35], v[34:35], v[64:65]
	v_pk_add_f32 v[32:33], v[32:33], v[58:59]
	v_pk_add_f32 v[30:31], v[30:31], v[66:67]
	v_pk_add_f32 v[28:29], v[28:29], v[52:53]
.LBB0_1530:
	v_readlane_b32 s4, v50, 4
	s_cmp_lt_i32 s4, 0
	s_cbranch_scc1 .LBB0_1532
	v_lshlrev_b32_e32 v61, 16, v104
	v_and_b32_e32 v60, 0xffff0000, v104
	v_lshlrev_b32_e32 v63, 16, v105
	v_and_b32_e32 v62, 0xffff0000, v105
	v_lshlrev_b32_e32 v55, 16, v106
	v_and_b32_e32 v54, 0xffff0000, v106
	v_lshlrev_b32_e32 v65, 16, v107
	v_and_b32_e32 v64, 0xffff0000, v107
	v_lshlrev_b32_e32 v57, 16, v108
	v_and_b32_e32 v56, 0xffff0000, v108
	v_lshlrev_b32_e32 v67, 16, v109
	v_and_b32_e32 v66, 0xffff0000, v109
	v_lshlrev_b32_e32 v59, 16, v110
	v_and_b32_e32 v58, 0xffff0000, v110
	v_lshlrev_b32_e32 v69, 16, v111
	v_and_b32_e32 v68, 0xffff0000, v111
	v_pk_add_f32 v[42:43], v[42:43], v[60:61]
	v_pk_add_f32 v[40:41], v[40:41], v[62:63]
	v_pk_add_f32 v[38:39], v[38:39], v[54:55]
	v_pk_add_f32 v[36:37], v[36:37], v[64:65]
	v_pk_add_f32 v[34:35], v[34:35], v[56:57]
	v_pk_add_f32 v[32:33], v[32:33], v[66:67]
	v_pk_add_f32 v[30:31], v[30:31], v[58:59]
	v_pk_add_f32 v[28:29], v[28:29], v[68:69]
.LBB0_1532:
	v_readlane_b32 s4, v50, 5
	s_cmp_lt_i32 s4, 0
	s_cbranch_scc1 .LBB0_1534
	v_lshlrev_b32_e32 v61, 16, v112
	v_and_b32_e32 v60, 0xffff0000, v112
	v_lshlrev_b32_e32 v63, 16, v113
	v_and_b32_e32 v62, 0xffff0000, v113
	v_lshlrev_b32_e32 v55, 16, v114
	v_and_b32_e32 v54, 0xffff0000, v114
	v_lshlrev_b32_e32 v65, 16, v115
	v_and_b32_e32 v64, 0xffff0000, v115
	v_lshlrev_b32_e32 v57, 16, v116
	v_and_b32_e32 v56, 0xffff0000, v116
	v_lshlrev_b32_e32 v67, 16, v117
	v_and_b32_e32 v66, 0xffff0000, v117
	v_lshlrev_b32_e32 v59, 16, v118
	v_and_b32_e32 v58, 0xffff0000, v118
	v_lshlrev_b32_e32 v69, 16, v119
	v_and_b32_e32 v68, 0xffff0000, v119
	v_pk_add_f32 v[42:43], v[42:43], v[60:61]
	v_pk_add_f32 v[40:41], v[40:41], v[62:63]
	v_pk_add_f32 v[38:39], v[38:39], v[54:55]
	v_pk_add_f32 v[36:37], v[36:37], v[64:65]
	v_pk_add_f32 v[34:35], v[34:35], v[56:57]
	v_pk_add_f32 v[32:33], v[32:33], v[66:67]
	v_pk_add_f32 v[30:31], v[30:31], v[58:59]
	v_pk_add_f32 v[28:29], v[28:29], v[68:69]
.LBB0_1534:
	v_readlane_b32 s4, v50, 6
	s_cmp_lt_i32 s4, 0
	s_cbranch_scc1 .LBB0_1536
	v_and_b32_e32 v60, 0xffff0000, v120
	v_lshlrev_b32_e32 v61, 16, v120
	v_and_b32_e32 v54, 0xffff0000, v121
	v_lshlrev_b32_e32 v55, 16, v121
	v_and_b32_e32 v62, 0xffff0000, v122
	v_lshlrev_b32_e32 v63, 16, v122
	v_and_b32_e32 v56, 0xffff0000, v123
	v_lshlrev_b32_e32 v57, 16, v123
	v_and_b32_e32 v64, 0xffff0000, v124
	v_lshlrev_b32_e32 v65, 16, v124
	v_and_b32_e32 v58, 0xffff0000, v125
	v_lshlrev_b32_e32 v59, 16, v125
	v_and_b32_e32 v66, 0xffff0000, v126
	v_lshlrev_b32_e32 v67, 16, v126
	v_and_b32_e32 v52, 0xffff0000, v127
	v_lshlrev_b32_e32 v53, 16, v127
	v_pk_add_f32 v[42:43], v[42:43], v[60:61]
	v_pk_add_f32 v[40:41], v[40:41], v[54:55]
	v_pk_add_f32 v[38:39], v[38:39], v[62:63]
	v_pk_add_f32 v[36:37], v[36:37], v[56:57]
	v_pk_add_f32 v[34:35], v[34:35], v[64:65]
	v_pk_add_f32 v[32:33], v[32:33], v[58:59]
	v_pk_add_f32 v[30:31], v[30:31], v[66:67]
	v_pk_add_f32 v[28:29], v[28:29], v[52:53]
.LBB0_1536:
	v_readlane_b32 s4, v50, 7
	s_cmp_lt_i32 s4, 0
	s_cbranch_scc1 .LBB0_1538
	v_and_b32_e32 v60, 0xffff0000, v128
	v_lshlrev_b32_e32 v61, 16, v128
	v_and_b32_e32 v54, 0xffff0000, v129
	v_lshlrev_b32_e32 v55, 16, v129
	v_and_b32_e32 v62, 0xffff0000, v130
	v_lshlrev_b32_e32 v63, 16, v130
	v_and_b32_e32 v56, 0xffff0000, v131
	v_lshlrev_b32_e32 v57, 16, v131
	v_and_b32_e32 v64, 0xffff0000, v132
	v_lshlrev_b32_e32 v65, 16, v132
	v_and_b32_e32 v58, 0xffff0000, v133
	v_lshlrev_b32_e32 v59, 16, v133
	v_and_b32_e32 v66, 0xffff0000, v134
	v_lshlrev_b32_e32 v67, 16, v134
	v_and_b32_e32 v52, 0xffff0000, v135
	v_lshlrev_b32_e32 v53, 16, v135
	v_pk_add_f32 v[42:43], v[42:43], v[60:61]
	v_pk_add_f32 v[40:41], v[40:41], v[54:55]
	v_pk_add_f32 v[38:39], v[38:39], v[62:63]
	v_pk_add_f32 v[36:37], v[36:37], v[56:57]
	v_pk_add_f32 v[34:35], v[34:35], v[64:65]
	v_pk_add_f32 v[32:33], v[32:33], v[58:59]
	v_pk_add_f32 v[30:31], v[30:31], v[66:67]
	v_pk_add_f32 v[28:29], v[28:29], v[52:53]
.LBB0_1538:
	v_readlane_b32 s4, v50, 8
	s_cmp_lt_i32 s4, 0
	s_cbranch_scc1 .LBB0_1540
	v_and_b32_e32 v60, 0xffff0000, v136
	v_lshlrev_b32_e32 v61, 16, v136
	v_and_b32_e32 v54, 0xffff0000, v137
	v_lshlrev_b32_e32 v55, 16, v137
	v_and_b32_e32 v62, 0xffff0000, v138
	v_lshlrev_b32_e32 v63, 16, v138
	v_and_b32_e32 v56, 0xffff0000, v139
	v_lshlrev_b32_e32 v57, 16, v139
	v_and_b32_e32 v64, 0xffff0000, v140
	v_lshlrev_b32_e32 v65, 16, v140
	v_and_b32_e32 v58, 0xffff0000, v141
	v_lshlrev_b32_e32 v59, 16, v141
	v_and_b32_e32 v66, 0xffff0000, v142
	v_lshlrev_b32_e32 v67, 16, v142
	v_and_b32_e32 v52, 0xffff0000, v143
	v_lshlrev_b32_e32 v53, 16, v143
	v_pk_add_f32 v[42:43], v[42:43], v[60:61]
	v_pk_add_f32 v[40:41], v[40:41], v[54:55]
	v_pk_add_f32 v[38:39], v[38:39], v[62:63]
	v_pk_add_f32 v[36:37], v[36:37], v[56:57]
	v_pk_add_f32 v[34:35], v[34:35], v[64:65]
	v_pk_add_f32 v[32:33], v[32:33], v[58:59]
	v_pk_add_f32 v[30:31], v[30:31], v[66:67]
	v_pk_add_f32 v[28:29], v[28:29], v[52:53]
.LBB0_1540:
	v_readlane_b32 s4, v50, 9
	s_cmp_lt_i32 s4, 0
	s_cbranch_scc1 .LBB0_1542
	v_and_b32_e32 v60, 0xffff0000, v144
	v_lshlrev_b32_e32 v61, 16, v144
	v_and_b32_e32 v54, 0xffff0000, v145
	v_lshlrev_b32_e32 v55, 16, v145
	v_and_b32_e32 v62, 0xffff0000, v146
	v_lshlrev_b32_e32 v63, 16, v146
	v_and_b32_e32 v56, 0xffff0000, v147
	v_lshlrev_b32_e32 v57, 16, v147
	v_and_b32_e32 v64, 0xffff0000, v148
	v_lshlrev_b32_e32 v65, 16, v148
	v_and_b32_e32 v58, 0xffff0000, v149
	v_lshlrev_b32_e32 v59, 16, v149
	v_and_b32_e32 v66, 0xffff0000, v150
	v_lshlrev_b32_e32 v67, 16, v150
	v_and_b32_e32 v52, 0xffff0000, v151
	v_lshlrev_b32_e32 v53, 16, v151
	v_pk_add_f32 v[42:43], v[42:43], v[60:61]
	v_pk_add_f32 v[40:41], v[40:41], v[54:55]
	v_pk_add_f32 v[38:39], v[38:39], v[62:63]
	v_pk_add_f32 v[36:37], v[36:37], v[56:57]
	v_pk_add_f32 v[34:35], v[34:35], v[64:65]
	v_pk_add_f32 v[32:33], v[32:33], v[58:59]
	v_pk_add_f32 v[30:31], v[30:31], v[66:67]
	v_pk_add_f32 v[28:29], v[28:29], v[52:53]
.LBB0_1542:
	v_readlane_b32 s4, v50, 10
	s_cmp_lt_i32 s4, 0
	s_cbranch_scc1 .LBB0_1544
	v_lshlrev_b32_e32 v61, 16, v152
	v_and_b32_e32 v60, 0xffff0000, v152
	v_lshlrev_b32_e32 v63, 16, v153
	v_and_b32_e32 v62, 0xffff0000, v153
	v_lshlrev_b32_e32 v55, 16, v154
	v_and_b32_e32 v54, 0xffff0000, v154
	v_lshlrev_b32_e32 v65, 16, v155
	v_and_b32_e32 v64, 0xffff0000, v155
	v_lshlrev_b32_e32 v57, 16, v156
	v_and_b32_e32 v56, 0xffff0000, v156
	v_lshlrev_b32_e32 v67, 16, v157
	v_and_b32_e32 v66, 0xffff0000, v157
	v_lshlrev_b32_e32 v59, 16, v158
	v_and_b32_e32 v58, 0xffff0000, v158
	v_lshlrev_b32_e32 v69, 16, v159
	v_and_b32_e32 v68, 0xffff0000, v159
	v_pk_add_f32 v[42:43], v[42:43], v[60:61]
	v_pk_add_f32 v[40:41], v[40:41], v[62:63]
	v_pk_add_f32 v[38:39], v[38:39], v[54:55]
	v_pk_add_f32 v[36:37], v[36:37], v[64:65]
	v_pk_add_f32 v[34:35], v[34:35], v[56:57]
	v_pk_add_f32 v[32:33], v[32:33], v[66:67]
	v_pk_add_f32 v[30:31], v[30:31], v[58:59]
	v_pk_add_f32 v[28:29], v[28:29], v[68:69]
.LBB0_1544:
	v_readlane_b32 s4, v50, 11
	s_cmp_lt_i32 s4, 0
	s_cbranch_scc1 .LBB0_1546
	v_lshlrev_b32_e32 v61, 16, v160
	v_and_b32_e32 v60, 0xffff0000, v160
	v_lshlrev_b32_e32 v63, 16, v161
	v_and_b32_e32 v62, 0xffff0000, v161
	v_lshlrev_b32_e32 v55, 16, v162
	v_and_b32_e32 v54, 0xffff0000, v162
	v_lshlrev_b32_e32 v65, 16, v163
	v_and_b32_e32 v64, 0xffff0000, v163
	v_lshlrev_b32_e32 v57, 16, v164
	v_and_b32_e32 v56, 0xffff0000, v164
	v_lshlrev_b32_e32 v67, 16, v165
	v_and_b32_e32 v66, 0xffff0000, v165
	v_lshlrev_b32_e32 v59, 16, v166
	v_and_b32_e32 v58, 0xffff0000, v166
	v_lshlrev_b32_e32 v69, 16, v167
	v_and_b32_e32 v68, 0xffff0000, v167
	v_pk_add_f32 v[42:43], v[42:43], v[60:61]
	v_pk_add_f32 v[40:41], v[40:41], v[62:63]
	v_pk_add_f32 v[38:39], v[38:39], v[54:55]
	v_pk_add_f32 v[36:37], v[36:37], v[64:65]
	v_pk_add_f32 v[34:35], v[34:35], v[56:57]
	v_pk_add_f32 v[32:33], v[32:33], v[66:67]
	v_pk_add_f32 v[30:31], v[30:31], v[58:59]
	v_pk_add_f32 v[28:29], v[28:29], v[68:69]
.LBB0_1546:
	v_readlane_b32 s4, v50, 12
	s_cmp_lt_i32 s4, 0
	s_cbranch_scc1 .LBB0_1548
	v_and_b32_e32 v60, 0xffff0000, v168
	v_lshlrev_b32_e32 v61, 16, v168
	v_and_b32_e32 v54, 0xffff0000, v169
	v_lshlrev_b32_e32 v55, 16, v169
	v_and_b32_e32 v62, 0xffff0000, v170
	v_lshlrev_b32_e32 v63, 16, v170
	v_and_b32_e32 v56, 0xffff0000, v171
	v_lshlrev_b32_e32 v57, 16, v171
	v_and_b32_e32 v64, 0xffff0000, v172
	v_lshlrev_b32_e32 v65, 16, v172
	v_and_b32_e32 v58, 0xffff0000, v173
	v_lshlrev_b32_e32 v59, 16, v173
	v_and_b32_e32 v66, 0xffff0000, v174
	v_lshlrev_b32_e32 v67, 16, v174
	v_and_b32_e32 v52, 0xffff0000, v175
	v_lshlrev_b32_e32 v53, 16, v175
	v_pk_add_f32 v[42:43], v[42:43], v[60:61]
	v_pk_add_f32 v[40:41], v[40:41], v[54:55]
	v_pk_add_f32 v[38:39], v[38:39], v[62:63]
	v_pk_add_f32 v[36:37], v[36:37], v[56:57]
	v_pk_add_f32 v[34:35], v[34:35], v[64:65]
	v_pk_add_f32 v[32:33], v[32:33], v[58:59]
	v_pk_add_f32 v[30:31], v[30:31], v[66:67]
	v_pk_add_f32 v[28:29], v[28:29], v[52:53]
.LBB0_1548:
	v_readlane_b32 s4, v50, 13
	s_cmp_lt_i32 s4, 0
	s_cbranch_scc1 .LBB0_1550
	v_and_b32_e32 v60, 0xffff0000, v176
	v_lshlrev_b32_e32 v61, 16, v176
	v_and_b32_e32 v54, 0xffff0000, v177
	v_lshlrev_b32_e32 v55, 16, v177
	v_and_b32_e32 v62, 0xffff0000, v178
	v_lshlrev_b32_e32 v63, 16, v178
	v_and_b32_e32 v56, 0xffff0000, v179
	v_lshlrev_b32_e32 v57, 16, v179
	v_and_b32_e32 v64, 0xffff0000, v180
	v_lshlrev_b32_e32 v65, 16, v180
	v_and_b32_e32 v58, 0xffff0000, v181
	v_lshlrev_b32_e32 v59, 16, v181
	v_and_b32_e32 v66, 0xffff0000, v182
	v_lshlrev_b32_e32 v67, 16, v182
	v_and_b32_e32 v52, 0xffff0000, v183
	v_lshlrev_b32_e32 v53, 16, v183
	v_pk_add_f32 v[42:43], v[42:43], v[60:61]
	v_pk_add_f32 v[40:41], v[40:41], v[54:55]
	v_pk_add_f32 v[38:39], v[38:39], v[62:63]
	v_pk_add_f32 v[36:37], v[36:37], v[56:57]
	v_pk_add_f32 v[34:35], v[34:35], v[64:65]
	v_pk_add_f32 v[32:33], v[32:33], v[58:59]
	v_pk_add_f32 v[30:31], v[30:31], v[66:67]
	v_pk_add_f32 v[28:29], v[28:29], v[52:53]
.LBB0_1550:
	v_readlane_b32 s4, v50, 14
	s_cmp_lt_i32 s4, 0
	s_cbranch_scc1 .LBB0_1552
	v_and_b32_e32 v60, 0xffff0000, v184
	v_lshlrev_b32_e32 v61, 16, v184
	v_and_b32_e32 v54, 0xffff0000, v185
	v_lshlrev_b32_e32 v55, 16, v185
	v_and_b32_e32 v62, 0xffff0000, v186
	v_lshlrev_b32_e32 v63, 16, v186
	v_and_b32_e32 v56, 0xffff0000, v187
	v_lshlrev_b32_e32 v57, 16, v187
	v_and_b32_e32 v64, 0xffff0000, v188
	v_lshlrev_b32_e32 v65, 16, v188
	v_and_b32_e32 v58, 0xffff0000, v189
	v_lshlrev_b32_e32 v59, 16, v189
	v_and_b32_e32 v66, 0xffff0000, v190
	v_lshlrev_b32_e32 v67, 16, v190
	v_and_b32_e32 v52, 0xffff0000, v191
	v_lshlrev_b32_e32 v53, 16, v191
	v_pk_add_f32 v[42:43], v[42:43], v[60:61]
	v_pk_add_f32 v[40:41], v[40:41], v[54:55]
	v_pk_add_f32 v[38:39], v[38:39], v[62:63]
	v_pk_add_f32 v[36:37], v[36:37], v[56:57]
	v_pk_add_f32 v[34:35], v[34:35], v[64:65]
	v_pk_add_f32 v[32:33], v[32:33], v[58:59]
	v_pk_add_f32 v[30:31], v[30:31], v[66:67]
	v_pk_add_f32 v[28:29], v[28:29], v[52:53]
.LBB0_1552:
	v_readlane_b32 s4, v50, 15
	s_cmp_lt_i32 s4, 0
	s_cbranch_scc1 .LBB0_1521
	v_and_b32_e32 v58, 0xffff0000, v192
	v_lshlrev_b32_e32 v59, 16, v192
	v_and_b32_e32 v52, 0xffff0000, v193
	v_lshlrev_b32_e32 v53, 16, v193
	v_and_b32_e32 v60, 0xffff0000, v194
	v_lshlrev_b32_e32 v61, 16, v194
	v_and_b32_e32 v54, 0xffff0000, v195
	v_lshlrev_b32_e32 v55, 16, v195
	v_and_b32_e32 v62, 0xffff0000, v196
	v_lshlrev_b32_e32 v63, 16, v196
	v_and_b32_e32 v56, 0xffff0000, v197
	v_lshlrev_b32_e32 v57, 16, v197
	v_and_b32_e32 v64, 0xffff0000, v198
	v_lshlrev_b32_e32 v65, 16, v198
	v_and_b32_e32 v50, 0xffff0000, v199
	v_lshlrev_b32_e32 v51, 16, v199
	v_pk_add_f32 v[42:43], v[42:43], v[58:59]
	v_pk_add_f32 v[40:41], v[40:41], v[52:53]
	v_pk_add_f32 v[38:39], v[38:39], v[60:61]
	v_pk_add_f32 v[36:37], v[36:37], v[54:55]
	v_pk_add_f32 v[34:35], v[34:35], v[62:63]
	v_pk_add_f32 v[32:33], v[32:33], v[56:57]
	v_pk_add_f32 v[30:31], v[30:31], v[64:65]
	v_pk_add_f32 v[28:29], v[28:29], v[50:51]
	s_branch .LBB0_1521

.LBB0_2782:
	v_lshl_add_u64 v[26:27], s[48:49], 0, v[22:23]
	v_add_co_u32_e32 v26, vcc, 0x800000, v26
	v_lshl_add_u64 v[28:29], s[48:49], 0, v[20:21]
	global_load_dword v48, v[28:29], off
	v_addc_co_u32_e32 v27, vcc, 0, v27, vcc
	global_load_dwordx2 v[28:29], v[26:27], off
	global_load_dwordx2 v[30:31], v[26:27], off offset:512
	global_load_dwordx2 v[32:33], v[26:27], off offset:1024
	global_load_dwordx2 v[50:51], v[26:27], off offset:1536
	s_waitcnt vmcnt(3)
	v_and_b32_e32 v38, 0xffff0000, v28
	v_readlane_b32 s0, v48, 0
	s_cmp_lt_i32 s0, 0
	v_lshlrev_b32_e32 v39, 16, v28
	v_and_b32_e32 v40, 0xffff0000, v29
	v_lshlrev_b32_e32 v41, 16, v29
	s_waitcnt vmcnt(2)
	v_and_b32_e32 v34, 0xffff0000, v30
	v_lshlrev_b32_e32 v35, 16, v30
	v_and_b32_e32 v36, 0xffff0000, v31
	v_lshlrev_b32_e32 v37, 16, v31
	s_waitcnt vmcnt(1)
	v_and_b32_e32 v30, 0xffff0000, v32
	v_lshlrev_b32_e32 v31, 16, v32
	v_and_b32_e32 v32, 0xffff0000, v33
	v_lshlrev_b32_e32 v33, 16, v33
	s_waitcnt vmcnt(0)
	v_readlane_b32 s0, v48, 0
	s_cmp_lt_i32 s0, 0
	s_cbranch_scc1 .Lcnb_0
	s_lshl_b64 s[12:13], s[0:1], 11
	v_lshl_add_u64 v[200:201], v[0:1], 0, s[12:13]
	global_load_dwordx2 v[72:73], v[200:201], off
	global_load_dwordx2 v[74:75], v[200:201], off offset:512
	global_load_dwordx2 v[76:77], v[200:201], off offset:1024
	global_load_dwordx2 v[78:79], v[200:201], off offset:1536
.Lcnb_0:
	v_readlane_b32 s0, v48, 1
	s_cmp_lt_i32 s0, 0
	s_cbranch_scc1 .Lcnb_1
	s_lshl_b64 s[12:13], s[0:1], 11
	v_lshl_add_u64 v[200:201], v[0:1], 0, s[12:13]
	global_load_dwordx2 v[80:81], v[200:201], off
	global_load_dwordx2 v[82:83], v[200:201], off offset:512
	global_load_dwordx2 v[84:85], v[200:201], off offset:1024
	global_load_dwordx2 v[86:87], v[200:201], off offset:1536
.Lcnb_1:
	v_readlane_b32 s0, v48, 2
	s_cmp_lt_i32 s0, 0
	s_cbranch_scc1 .Lcnb_2
	s_lshl_b64 s[12:13], s[0:1], 11
	v_lshl_add_u64 v[200:201], v[0:1], 0, s[12:13]
	global_load_dwordx2 v[88:89], v[200:201], off
	global_load_dwordx2 v[90:91], v[200:201], off offset:512
	global_load_dwordx2 v[92:93], v[200:201], off offset:1024
	global_load_dwordx2 v[94:95], v[200:201], off offset:1536
.Lcnb_2:
	v_readlane_b32 s0, v48, 3
	s_cmp_lt_i32 s0, 0
	s_cbranch_scc1 .Lcnb_3
	s_lshl_b64 s[12:13], s[0:1], 11
	v_lshl_add_u64 v[200:201], v[0:1], 0, s[12:13]
	global_load_dwordx2 v[96:97], v[200:201], off
	global_load_dwordx2 v[98:99], v[200:201], off offset:512
	global_load_dwordx2 v[100:101], v[200:201], off offset:1024
	global_load_dwordx2 v[102:103], v[200:201], off offset:1536
.Lcnb_3:
	v_readlane_b32 s0, v48, 4
	s_cmp_lt_i32 s0, 0
	s_cbranch_scc1 .Lcnb_4
	s_lshl_b64 s[12:13], s[0:1], 11
	v_lshl_add_u64 v[200:201], v[0:1], 0, s[12:13]
	global_load_dwordx2 v[104:105], v[200:201], off
	global_load_dwordx2 v[106:107], v[200:201], off offset:512
	global_load_dwordx2 v[108:109], v[200:201], off offset:1024
	global_load_dwordx2 v[110:111], v[200:201], off offset:1536
.Lcnb_4:
	v_readlane_b32 s0, v48, 5
	s_cmp_lt_i32 s0, 0
	s_cbranch_scc1 .Lcnb_5
	s_lshl_b64 s[12:13], s[0:1], 11
	v_lshl_add_u64 v[200:201], v[0:1], 0, s[12:13]
	global_load_dwordx2 v[112:113], v[200:201], off
	global_load_dwordx2 v[114:115], v[200:201], off offset:512
	global_load_dwordx2 v[116:117], v[200:201], off offset:1024
	global_load_dwordx2 v[118:119], v[200:201], off offset:1536
.Lcnb_5:
	v_readlane_b32 s0, v48, 6
	s_cmp_lt_i32 s0, 0
	s_cbranch_scc1 .Lcnb_6
	s_lshl_b64 s[12:13], s[0:1], 11
	v_lshl_add_u64 v[200:201], v[0:1], 0, s[12:13]
	global_load_dwordx2 v[120:121], v[200:201], off
	global_load_dwordx2 v[122:123], v[200:201], off offset:512
	global_load_dwordx2 v[124:125], v[200:201], off offset:1024
	global_load_dwordx2 v[126:127], v[200:201], off offset:1536
.Lcnb_6:
	v_readlane_b32 s0, v48, 7
	s_cmp_lt_i32 s0, 0
	s_cbranch_scc1 .Lcnb_7
	s_lshl_b64 s[12:13], s[0:1], 11
	v_lshl_add_u64 v[200:201], v[0:1], 0, s[12:13]
	global_load_dwordx2 v[128:129], v[200:201], off
	global_load_dwordx2 v[130:131], v[200:201], off offset:512
	global_load_dwordx2 v[132:133], v[200:201], off offset:1024
	global_load_dwordx2 v[134:135], v[200:201], off offset:1536
.Lcnb_7:
	v_readlane_b32 s0, v48, 8
	s_cmp_lt_i32 s0, 0
	s_cbranch_scc1 .Lcnb_8
	s_lshl_b64 s[12:13], s[0:1], 11
	v_lshl_add_u64 v[200:201], v[0:1], 0, s[12:13]
	global_load_dwordx2 v[136:137], v[200:201], off
	global_load_dwordx2 v[138:139], v[200:201], off offset:512
	global_load_dwordx2 v[140:141], v[200:201], off offset:1024
	global_load_dwordx2 v[142:143], v[200:201], off offset:1536
.Lcnb_8:
	v_readlane_b32 s0, v48, 9
	s_cmp_lt_i32 s0, 0
	s_cbranch_scc1 .Lcnb_9
	s_lshl_b64 s[12:13], s[0:1], 11
	v_lshl_add_u64 v[200:201], v[0:1], 0, s[12:13]
	global_load_dwordx2 v[144:145], v[200:201], off
	global_load_dwordx2 v[146:147], v[200:201], off offset:512
	global_load_dwordx2 v[148:149], v[200:201], off offset:1024
	global_load_dwordx2 v[150:151], v[200:201], off offset:1536
.Lcnb_9:
	v_readlane_b32 s0, v48, 10
	s_cmp_lt_i32 s0, 0
	s_cbranch_scc1 .Lcnb_10
	s_lshl_b64 s[12:13], s[0:1], 11
	v_lshl_add_u64 v[200:201], v[0:1], 0, s[12:13]
	global_load_dwordx2 v[152:153], v[200:201], off
	global_load_dwordx2 v[154:155], v[200:201], off offset:512
	global_load_dwordx2 v[156:157], v[200:201], off offset:1024
	global_load_dwordx2 v[158:159], v[200:201], off offset:1536
.Lcnb_10:
	v_readlane_b32 s0, v48, 11
	s_cmp_lt_i32 s0, 0
	s_cbranch_scc1 .Lcnb_11
	s_lshl_b64 s[12:13], s[0:1], 11
	v_lshl_add_u64 v[200:201], v[0:1], 0, s[12:13]
	global_load_dwordx2 v[160:161], v[200:201], off
	global_load_dwordx2 v[162:163], v[200:201], off offset:512
	global_load_dwordx2 v[164:165], v[200:201], off offset:1024
	global_load_dwordx2 v[166:167], v[200:201], off offset:1536
.Lcnb_11:
	v_readlane_b32 s0, v48, 12
	s_cmp_lt_i32 s0, 0
	s_cbranch_scc1 .Lcnb_12
	s_lshl_b64 s[12:13], s[0:1], 11
	v_lshl_add_u64 v[200:201], v[0:1], 0, s[12:13]
	global_load_dwordx2 v[168:169], v[200:201], off
	global_load_dwordx2 v[170:171], v[200:201], off offset:512
	global_load_dwordx2 v[172:173], v[200:201], off offset:1024
	global_load_dwordx2 v[174:175], v[200:201], off offset:1536
.Lcnb_12:
	v_readlane_b32 s0, v48, 13
	s_cmp_lt_i32 s0, 0
	s_cbranch_scc1 .Lcnb_13
	s_lshl_b64 s[12:13], s[0:1], 11
	v_lshl_add_u64 v[200:201], v[0:1], 0, s[12:13]
	global_load_dwordx2 v[176:177], v[200:201], off
	global_load_dwordx2 v[178:179], v[200:201], off offset:512
	global_load_dwordx2 v[180:181], v[200:201], off offset:1024
	global_load_dwordx2 v[182:183], v[200:201], off offset:1536
.Lcnb_13:
	v_readlane_b32 s0, v48, 14
	s_cmp_lt_i32 s0, 0
	s_cbranch_scc1 .Lcnb_14
	s_lshl_b64 s[12:13], s[0:1], 11
	v_lshl_add_u64 v[200:201], v[0:1], 0, s[12:13]
	global_load_dwordx2 v[184:185], v[200:201], off
	global_load_dwordx2 v[186:187], v[200:201], off offset:512
	global_load_dwordx2 v[188:189], v[200:201], off offset:1024
	global_load_dwordx2 v[190:191], v[200:201], off offset:1536
.Lcnb_14:
	v_readlane_b32 s0, v48, 15
	s_cmp_lt_i32 s0, 0
	s_cbranch_scc1 .Lcnb_15
	s_lshl_b64 s[12:13], s[0:1], 11
	v_lshl_add_u64 v[200:201], v[0:1], 0, s[12:13]
	global_load_dwordx2 v[192:193], v[200:201], off
	global_load_dwordx2 v[194:195], v[200:201], off offset:512
	global_load_dwordx2 v[196:197], v[200:201], off offset:1024
	global_load_dwordx2 v[198:199], v[200:201], off offset:1536
.Lcnb_15:
	v_readlane_b32 s0, v48, 0
	s_cmp_lt_i32 s0, 0
	s_waitcnt vmcnt(0)
	v_and_b32_e32 v26, 0xffff0000, v50
	v_lshlrev_b32_e32 v27, 16, v50
	v_and_b32_e32 v28, 0xffff0000, v51
	v_lshlrev_b32_e32 v29, 16, v51
	s_cbranch_scc1 .LBB0_2784
	v_and_b32_e32 v50, 0xffff0000, v72
	v_lshlrev_b32_e32 v51, 16, v72
	v_and_b32_e32 v52, 0xffff0000, v73
	v_lshlrev_b32_e32 v53, 16, v73
	v_and_b32_e32 v60, 0xffff0000, v74
	v_lshlrev_b32_e32 v61, 16, v74
	v_and_b32_e32 v54, 0xffff0000, v75
	v_lshlrev_b32_e32 v55, 16, v75
	v_and_b32_e32 v62, 0xffff0000, v76
	v_lshlrev_b32_e32 v63, 16, v76
	v_and_b32_e32 v56, 0xffff0000, v77
	v_lshlrev_b32_e32 v57, 16, v77
	v_and_b32_e32 v64, 0xffff0000, v78
	v_lshlrev_b32_e32 v65, 16, v78
	v_and_b32_e32 v58, 0xffff0000, v79
	v_lshlrev_b32_e32 v59, 16, v79
	v_pk_add_f32 v[38:39], v[38:39], v[50:51]
	v_pk_add_f32 v[40:41], v[40:41], v[52:53]
	v_pk_add_f32 v[34:35], v[34:35], v[60:61]
	v_pk_add_f32 v[36:37], v[36:37], v[54:55]
	v_pk_add_f32 v[30:31], v[30:31], v[62:63]
	v_pk_add_f32 v[32:33], v[32:33], v[56:57]
	v_pk_add_f32 v[26:27], v[26:27], v[64:65]
	v_pk_add_f32 v[28:29], v[28:29], v[58:59]
.LBB0_2784:
	v_readlane_b32 s0, v48, 1
	s_cmp_lt_i32 s0, 0
	s_cbranch_scc1 .LBB0_2786
	v_and_b32_e32 v50, 0xffff0000, v80
	v_lshlrev_b32_e32 v51, 16, v80
	v_and_b32_e32 v52, 0xffff0000, v81
	v_lshlrev_b32_e32 v53, 16, v81
	v_and_b32_e32 v60, 0xffff0000, v82
	v_lshlrev_b32_e32 v61, 16, v82
	v_and_b32_e32 v54, 0xffff0000, v83
	v_lshlrev_b32_e32 v55, 16, v83
	v_and_b32_e32 v62, 0xffff0000, v84
	v_lshlrev_b32_e32 v63, 16, v84
	v_and_b32_e32 v56, 0xffff0000, v85
	v_lshlrev_b32_e32 v57, 16, v85
	v_and_b32_e32 v64, 0xffff0000, v86
	v_lshlrev_b32_e32 v65, 16, v86
	v_and_b32_e32 v58, 0xffff0000, v87
	v_lshlrev_b32_e32 v59, 16, v87
	v_pk_add_f32 v[38:39], v[38:39], v[50:51]
	v_pk_add_f32 v[40:41], v[40:41], v[52:53]
	v_pk_add_f32 v[34:35], v[34:35], v[60:61]
	v_pk_add_f32 v[36:37], v[36:37], v[54:55]
	v_pk_add_f32 v[30:31], v[30:31], v[62:63]
	v_pk_add_f32 v[32:33], v[32:33], v[56:57]
	v_pk_add_f32 v[26:27], v[26:27], v[64:65]
	v_pk_add_f32 v[28:29], v[28:29], v[58:59]
.LBB0_2786:
	v_readlane_b32 s0, v48, 2
	s_cmp_lt_i32 s0, 0
	s_cbranch_scc1 .LBB0_2788
	v_and_b32_e32 v50, 0xffff0000, v88
	v_lshlrev_b32_e32 v51, 16, v88
	v_and_b32_e32 v52, 0xffff0000, v89
	v_lshlrev_b32_e32 v53, 16, v89
	v_and_b32_e32 v60, 0xffff0000, v90
	v_lshlrev_b32_e32 v61, 16, v90
	v_and_b32_e32 v54, 0xffff0000, v91
	v_lshlrev_b32_e32 v55, 16, v91
	v_and_b32_e32 v62, 0xffff0000, v92
	v_lshlrev_b32_e32 v63, 16, v92
	v_and_b32_e32 v56, 0xffff0000, v93
	v_lshlrev_b32_e32 v57, 16, v93
	v_and_b32_e32 v64, 0xffff0000, v94
	v_lshlrev_b32_e32 v65, 16, v94
	v_and_b32_e32 v58, 0xffff0000, v95
	v_lshlrev_b32_e32 v59, 16, v95
	v_pk_add_f32 v[38:39], v[38:39], v[50:51]
	v_pk_add_f32 v[40:41], v[40:41], v[52:53]
	v_pk_add_f32 v[34:35], v[34:35], v[60:61]
	v_pk_add_f32 v[36:37], v[36:37], v[54:55]
	v_pk_add_f32 v[30:31], v[30:31], v[62:63]
	v_pk_add_f32 v[32:33], v[32:33], v[56:57]
	v_pk_add_f32 v[26:27], v[26:27], v[64:65]
	v_pk_add_f32 v[28:29], v[28:29], v[58:59]
.LBB0_2788:
	v_readlane_b32 s0, v48, 3
	s_cmp_lt_i32 s0, 0
	s_cbranch_scc1 .LBB0_2790
	v_and_b32_e32 v50, 0xffff0000, v96
	v_lshlrev_b32_e32 v51, 16, v96
	v_and_b32_e32 v52, 0xffff0000, v97
	v_lshlrev_b32_e32 v53, 16, v97
	v_and_b32_e32 v60, 0xffff0000, v98
	v_lshlrev_b32_e32 v61, 16, v98
	v_and_b32_e32 v54, 0xffff0000, v99
	v_lshlrev_b32_e32 v55, 16, v99
	v_and_b32_e32 v62, 0xffff0000, v100
	v_lshlrev_b32_e32 v63, 16, v100
	v_and_b32_e32 v56, 0xffff0000, v101
	v_lshlrev_b32_e32 v57, 16, v101
	v_and_b32_e32 v64, 0xffff0000, v102
	v_lshlrev_b32_e32 v65, 16, v102
	v_and_b32_e32 v58, 0xffff0000, v103
	v_lshlrev_b32_e32 v59, 16, v103
	v_pk_add_f32 v[38:39], v[38:39], v[50:51]
	v_pk_add_f32 v[40:41], v[40:41], v[52:53]
	v_pk_add_f32 v[34:35], v[34:35], v[60:61]
	v_pk_add_f32 v[36:37], v[36:37], v[54:55]
	v_pk_add_f32 v[30:31], v[30:31], v[62:63]
	v_pk_add_f32 v[32:33], v[32:33], v[56:57]
	v_pk_add_f32 v[26:27], v[26:27], v[64:65]
	v_pk_add_f32 v[28:29], v[28:29], v[58:59]
.LBB0_2790:
	v_readlane_b32 s0, v48, 4
	s_cmp_lt_i32 s0, 0
	s_cbranch_scc1 .LBB0_2792
	v_lshlrev_b32_e32 v51, 16, v104
	v_and_b32_e32 v50, 0xffff0000, v104
	v_lshlrev_b32_e32 v61, 16, v105
	v_and_b32_e32 v60, 0xffff0000, v105
	v_lshlrev_b32_e32 v53, 16, v106
	v_and_b32_e32 v52, 0xffff0000, v106
	v_lshlrev_b32_e32 v63, 16, v107
	v_and_b32_e32 v62, 0xffff0000, v107
	v_lshlrev_b32_e32 v55, 16, v108
	v_and_b32_e32 v54, 0xffff0000, v108
	v_lshlrev_b32_e32 v65, 16, v109
	v_and_b32_e32 v64, 0xffff0000, v109
	v_lshlrev_b32_e32 v57, 16, v110
	v_and_b32_e32 v56, 0xffff0000, v110
	v_lshlrev_b32_e32 v67, 16, v111
	v_and_b32_e32 v66, 0xffff0000, v111
	v_pk_add_f32 v[38:39], v[38:39], v[50:51]
	v_pk_add_f32 v[40:41], v[40:41], v[60:61]
	v_pk_add_f32 v[34:35], v[34:35], v[52:53]
	v_pk_add_f32 v[36:37], v[36:37], v[62:63]
	v_pk_add_f32 v[30:31], v[30:31], v[54:55]
	v_pk_add_f32 v[32:33], v[32:33], v[64:65]
	v_pk_add_f32 v[26:27], v[26:27], v[56:57]
	v_pk_add_f32 v[28:29], v[28:29], v[66:67]
.LBB0_2792:
	v_readlane_b32 s0, v48, 5
	s_cmp_lt_i32 s0, 0
	s_cbranch_scc1 .LBB0_2794
	v_lshlrev_b32_e32 v51, 16, v112
	v_and_b32_e32 v50, 0xffff0000, v112
	v_lshlrev_b32_e32 v61, 16, v113
	v_and_b32_e32 v60, 0xffff0000, v113
	v_lshlrev_b32_e32 v53, 16, v114
	v_and_b32_e32 v52, 0xffff0000, v114
	v_lshlrev_b32_e32 v63, 16, v115
	v_and_b32_e32 v62, 0xffff0000, v115
	v_lshlrev_b32_e32 v55, 16, v116
	v_and_b32_e32 v54, 0xffff0000, v116
	v_lshlrev_b32_e32 v65, 16, v117
	v_and_b32_e32 v64, 0xffff0000, v117
	v_lshlrev_b32_e32 v57, 16, v118
	v_and_b32_e32 v56, 0xffff0000, v118
	v_lshlrev_b32_e32 v67, 16, v119
	v_and_b32_e32 v66, 0xffff0000, v119
	v_pk_add_f32 v[38:39], v[38:39], v[50:51]
	v_pk_add_f32 v[40:41], v[40:41], v[60:61]
	v_pk_add_f32 v[34:35], v[34:35], v[52:53]
	v_pk_add_f32 v[36:37], v[36:37], v[62:63]
	v_pk_add_f32 v[30:31], v[30:31], v[54:55]
	v_pk_add_f32 v[32:33], v[32:33], v[64:65]
	v_pk_add_f32 v[26:27], v[26:27], v[56:57]
	v_pk_add_f32 v[28:29], v[28:29], v[66:67]
.LBB0_2794:
	v_readlane_b32 s0, v48, 6
	s_cmp_lt_i32 s0, 0
	s_cbranch_scc1 .LBB0_2796
	v_and_b32_e32 v50, 0xffff0000, v120
	v_lshlrev_b32_e32 v51, 16, v120
	v_and_b32_e32 v52, 0xffff0000, v121
	v_lshlrev_b32_e32 v53, 16, v121
	v_and_b32_e32 v60, 0xffff0000, v122
	v_lshlrev_b32_e32 v61, 16, v122
	v_and_b32_e32 v54, 0xffff0000, v123
	v_lshlrev_b32_e32 v55, 16, v123
	v_and_b32_e32 v62, 0xffff0000, v124
	v_lshlrev_b32_e32 v63, 16, v124
	v_and_b32_e32 v56, 0xffff0000, v125
	v_lshlrev_b32_e32 v57, 16, v125
	v_and_b32_e32 v64, 0xffff0000, v126
	v_lshlrev_b32_e32 v65, 16, v126
	v_and_b32_e32 v58, 0xffff0000, v127
	v_lshlrev_b32_e32 v59, 16, v127
	v_pk_add_f32 v[38:39], v[38:39], v[50:51]
	v_pk_add_f32 v[40:41], v[40:41], v[52:53]
	v_pk_add_f32 v[34:35], v[34:35], v[60:61]
	v_pk_add_f32 v[36:37], v[36:37], v[54:55]
	v_pk_add_f32 v[30:31], v[30:31], v[62:63]
	v_pk_add_f32 v[32:33], v[32:33], v[56:57]
	v_pk_add_f32 v[26:27], v[26:27], v[64:65]
	v_pk_add_f32 v[28:29], v[28:29], v[58:59]
.LBB0_2796:
	v_readlane_b32 s0, v48, 7
	s_cmp_lt_i32 s0, 0
	s_cbranch_scc1 .LBB0_2798
	v_and_b32_e32 v50, 0xffff0000, v128
	v_lshlrev_b32_e32 v51, 16, v128
	v_and_b32_e32 v52, 0xffff0000, v129
	v_lshlrev_b32_e32 v53, 16, v129
	v_and_b32_e32 v60, 0xffff0000, v130
	v_lshlrev_b32_e32 v61, 16, v130
	v_and_b32_e32 v54, 0xffff0000, v131
	v_lshlrev_b32_e32 v55, 16, v131
	v_and_b32_e32 v62, 0xffff0000, v132
	v_lshlrev_b32_e32 v63, 16, v132
	v_and_b32_e32 v56, 0xffff0000, v133
	v_lshlrev_b32_e32 v57, 16, v133
	v_and_b32_e32 v64, 0xffff0000, v134
	v_lshlrev_b32_e32 v65, 16, v134
	v_and_b32_e32 v58, 0xffff0000, v135
	v_lshlrev_b32_e32 v59, 16, v135
	v_pk_add_f32 v[38:39], v[38:39], v[50:51]
	v_pk_add_f32 v[40:41], v[40:41], v[52:53]
	v_pk_add_f32 v[34:35], v[34:35], v[60:61]
	v_pk_add_f32 v[36:37], v[36:37], v[54:55]
	v_pk_add_f32 v[30:31], v[30:31], v[62:63]
	v_pk_add_f32 v[32:33], v[32:33], v[56:57]
	v_pk_add_f32 v[26:27], v[26:27], v[64:65]
	v_pk_add_f32 v[28:29], v[28:29], v[58:59]
.LBB0_2798:
	v_readlane_b32 s0, v48, 8
	s_cmp_lt_i32 s0, 0
	s_cbranch_scc1 .LBB0_2800
	v_and_b32_e32 v50, 0xffff0000, v136
	v_lshlrev_b32_e32 v51, 16, v136
	v_and_b32_e32 v52, 0xffff0000, v137
	v_lshlrev_b32_e32 v53, 16, v137
	v_and_b32_e32 v60, 0xffff0000, v138
	v_lshlrev_b32_e32 v61, 16, v138
	v_and_b32_e32 v54, 0xffff0000, v139
	v_lshlrev_b32_e32 v55, 16, v139
	v_and_b32_e32 v62, 0xffff0000, v140
	v_lshlrev_b32_e32 v63, 16, v140
	v_and_b32_e32 v56, 0xffff0000, v141
	v_lshlrev_b32_e32 v57, 16, v141
	v_and_b32_e32 v64, 0xffff0000, v142
	v_lshlrev_b32_e32 v65, 16, v142
	v_and_b32_e32 v58, 0xffff0000, v143
	v_lshlrev_b32_e32 v59, 16, v143
	v_pk_add_f32 v[38:39], v[38:39], v[50:51]
	v_pk_add_f32 v[40:41], v[40:41], v[52:53]
	v_pk_add_f32 v[34:35], v[34:35], v[60:61]
	v_pk_add_f32 v[36:37], v[36:37], v[54:55]
	v_pk_add_f32 v[30:31], v[30:31], v[62:63]
	v_pk_add_f32 v[32:33], v[32:33], v[56:57]
	v_pk_add_f32 v[26:27], v[26:27], v[64:65]
	v_pk_add_f32 v[28:29], v[28:29], v[58:59]
.LBB0_2800:
	v_readlane_b32 s0, v48, 9
	s_cmp_lt_i32 s0, 0
	s_cbranch_scc1 .LBB0_2802
	v_and_b32_e32 v50, 0xffff0000, v144
	v_lshlrev_b32_e32 v51, 16, v144
	v_and_b32_e32 v52, 0xffff0000, v145
	v_lshlrev_b32_e32 v53, 16, v145
	v_and_b32_e32 v60, 0xffff0000, v146
	v_lshlrev_b32_e32 v61, 16, v146
	v_and_b32_e32 v54, 0xffff0000, v147
	v_lshlrev_b32_e32 v55, 16, v147
	v_and_b32_e32 v62, 0xffff0000, v148
	v_lshlrev_b32_e32 v63, 16, v148
	v_and_b32_e32 v56, 0xffff0000, v149
	v_lshlrev_b32_e32 v57, 16, v149
	v_and_b32_e32 v64, 0xffff0000, v150
	v_lshlrev_b32_e32 v65, 16, v150
	v_and_b32_e32 v58, 0xffff0000, v151
	v_lshlrev_b32_e32 v59, 16, v151
	v_pk_add_f32 v[38:39], v[38:39], v[50:51]
	v_pk_add_f32 v[40:41], v[40:41], v[52:53]
	v_pk_add_f32 v[34:35], v[34:35], v[60:61]
	v_pk_add_f32 v[36:37], v[36:37], v[54:55]
	v_pk_add_f32 v[30:31], v[30:31], v[62:63]
	v_pk_add_f32 v[32:33], v[32:33], v[56:57]
	v_pk_add_f32 v[26:27], v[26:27], v[64:65]
	v_pk_add_f32 v[28:29], v[28:29], v[58:59]
.LBB0_2802:
	v_readlane_b32 s0, v48, 10
	s_cmp_lt_i32 s0, 0
	s_cbranch_scc1 .LBB0_2804
	v_lshlrev_b32_e32 v51, 16, v152
	v_and_b32_e32 v50, 0xffff0000, v152
	v_lshlrev_b32_e32 v61, 16, v153
	v_and_b32_e32 v60, 0xffff0000, v153
	v_lshlrev_b32_e32 v53, 16, v154
	v_and_b32_e32 v52, 0xffff0000, v154
	v_lshlrev_b32_e32 v63, 16, v155
	v_and_b32_e32 v62, 0xffff0000, v155
	v_lshlrev_b32_e32 v55, 16, v156
	v_and_b32_e32 v54, 0xffff0000, v156
	v_lshlrev_b32_e32 v65, 16, v157
	v_and_b32_e32 v64, 0xffff0000, v157
	v_lshlrev_b32_e32 v57, 16, v158
	v_and_b32_e32 v56, 0xffff0000, v158
	v_lshlrev_b32_e32 v67, 16, v159
	v_and_b32_e32 v66, 0xffff0000, v159
	v_pk_add_f32 v[38:39], v[38:39], v[50:51]
	v_pk_add_f32 v[40:41], v[40:41], v[60:61]
	v_pk_add_f32 v[34:35], v[34:35], v[52:53]
	v_pk_add_f32 v[36:37], v[36:37], v[62:63]
	v_pk_add_f32 v[30:31], v[30:31], v[54:55]
	v_pk_add_f32 v[32:33], v[32:33], v[64:65]
	v_pk_add_f32 v[26:27], v[26:27], v[56:57]
	v_pk_add_f32 v[28:29], v[28:29], v[66:67]
.LBB0_2804:
	v_readlane_b32 s0, v48, 11
	s_cmp_lt_i32 s0, 0
	s_cbranch_scc1 .LBB0_2806
	v_lshlrev_b32_e32 v51, 16, v160
	v_and_b32_e32 v50, 0xffff0000, v160
	v_lshlrev_b32_e32 v61, 16, v161
	v_and_b32_e32 v60, 0xffff0000, v161
	v_lshlrev_b32_e32 v53, 16, v162
	v_and_b32_e32 v52, 0xffff0000, v162
	v_lshlrev_b32_e32 v63, 16, v163
	v_and_b32_e32 v62, 0xffff0000, v163
	v_lshlrev_b32_e32 v55, 16, v164
	v_and_b32_e32 v54, 0xffff0000, v164
	v_lshlrev_b32_e32 v65, 16, v165
	v_and_b32_e32 v64, 0xffff0000, v165
	v_lshlrev_b32_e32 v57, 16, v166
	v_and_b32_e32 v56, 0xffff0000, v166
	v_lshlrev_b32_e32 v67, 16, v167
	v_and_b32_e32 v66, 0xffff0000, v167
	v_pk_add_f32 v[38:39], v[38:39], v[50:51]
	v_pk_add_f32 v[40:41], v[40:41], v[60:61]
	v_pk_add_f32 v[34:35], v[34:35], v[52:53]
	v_pk_add_f32 v[36:37], v[36:37], v[62:63]
	v_pk_add_f32 v[30:31], v[30:31], v[54:55]
	v_pk_add_f32 v[32:33], v[32:33], v[64:65]
	v_pk_add_f32 v[26:27], v[26:27], v[56:57]
	v_pk_add_f32 v[28:29], v[28:29], v[66:67]
.LBB0_2806:
	v_readlane_b32 s0, v48, 12
	s_cmp_lt_i32 s0, 0
	s_cbranch_scc1 .LBB0_2808
	v_and_b32_e32 v50, 0xffff0000, v168
	v_lshlrev_b32_e32 v51, 16, v168
	v_and_b32_e32 v52, 0xffff0000, v169
	v_lshlrev_b32_e32 v53, 16, v169
	v_and_b32_e32 v60, 0xffff0000, v170
	v_lshlrev_b32_e32 v61, 16, v170
	v_and_b32_e32 v54, 0xffff0000, v171
	v_lshlrev_b32_e32 v55, 16, v171
	v_and_b32_e32 v62, 0xffff0000, v172
	v_lshlrev_b32_e32 v63, 16, v172
	v_and_b32_e32 v56, 0xffff0000, v173
	v_lshlrev_b32_e32 v57, 16, v173
	v_and_b32_e32 v64, 0xffff0000, v174
	v_lshlrev_b32_e32 v65, 16, v174
	v_and_b32_e32 v58, 0xffff0000, v175
	v_lshlrev_b32_e32 v59, 16, v175
	v_pk_add_f32 v[38:39], v[38:39], v[50:51]
	v_pk_add_f32 v[40:41], v[40:41], v[52:53]
	v_pk_add_f32 v[34:35], v[34:35], v[60:61]
	v_pk_add_f32 v[36:37], v[36:37], v[54:55]
	v_pk_add_f32 v[30:31], v[30:31], v[62:63]
	v_pk_add_f32 v[32:33], v[32:33], v[56:57]
	v_pk_add_f32 v[26:27], v[26:27], v[64:65]
	v_pk_add_f32 v[28:29], v[28:29], v[58:59]
.LBB0_2808:
	v_readlane_b32 s0, v48, 13
	s_cmp_lt_i32 s0, 0
	s_cbranch_scc1 .LBB0_2810
	v_and_b32_e32 v50, 0xffff0000, v176
	v_lshlrev_b32_e32 v51, 16, v176
	v_and_b32_e32 v52, 0xffff0000, v177
	v_lshlrev_b32_e32 v53, 16, v177
	v_and_b32_e32 v60, 0xffff0000, v178
	v_lshlrev_b32_e32 v61, 16, v178
	v_and_b32_e32 v54, 0xffff0000, v179
	v_lshlrev_b32_e32 v55, 16, v179
	v_and_b32_e32 v62, 0xffff0000, v180
	v_lshlrev_b32_e32 v63, 16, v180
	v_and_b32_e32 v56, 0xffff0000, v181
	v_lshlrev_b32_e32 v57, 16, v181
	v_and_b32_e32 v64, 0xffff0000, v182
	v_lshlrev_b32_e32 v65, 16, v182
	v_and_b32_e32 v58, 0xffff0000, v183
	v_lshlrev_b32_e32 v59, 16, v183
	v_pk_add_f32 v[38:39], v[38:39], v[50:51]
	v_pk_add_f32 v[40:41], v[40:41], v[52:53]
	v_pk_add_f32 v[34:35], v[34:35], v[60:61]
	v_pk_add_f32 v[36:37], v[36:37], v[54:55]
	v_pk_add_f32 v[30:31], v[30:31], v[62:63]
	v_pk_add_f32 v[32:33], v[32:33], v[56:57]
	v_pk_add_f32 v[26:27], v[26:27], v[64:65]
	v_pk_add_f32 v[28:29], v[28:29], v[58:59]
.LBB0_2810:
	v_readlane_b32 s0, v48, 14
	s_cmp_lt_i32 s0, 0
	s_cbranch_scc1 .LBB0_2812
	v_and_b32_e32 v50, 0xffff0000, v184
	v_lshlrev_b32_e32 v51, 16, v184
	v_and_b32_e32 v52, 0xffff0000, v185
	v_lshlrev_b32_e32 v53, 16, v185
	v_and_b32_e32 v60, 0xffff0000, v186
	v_lshlrev_b32_e32 v61, 16, v186
	v_and_b32_e32 v54, 0xffff0000, v187
	v_lshlrev_b32_e32 v55, 16, v187
	v_and_b32_e32 v62, 0xffff0000, v188
	v_lshlrev_b32_e32 v63, 16, v188
	v_and_b32_e32 v56, 0xffff0000, v189
	v_lshlrev_b32_e32 v57, 16, v189
	v_and_b32_e32 v64, 0xffff0000, v190
	v_lshlrev_b32_e32 v65, 16, v190
	v_and_b32_e32 v58, 0xffff0000, v191
	v_lshlrev_b32_e32 v59, 16, v191
	v_pk_add_f32 v[38:39], v[38:39], v[50:51]
	v_pk_add_f32 v[40:41], v[40:41], v[52:53]
	v_pk_add_f32 v[34:35], v[34:35], v[60:61]
	v_pk_add_f32 v[36:37], v[36:37], v[54:55]
	v_pk_add_f32 v[30:31], v[30:31], v[62:63]
	v_pk_add_f32 v[32:33], v[32:33], v[56:57]
	v_pk_add_f32 v[26:27], v[26:27], v[64:65]
	v_pk_add_f32 v[28:29], v[28:29], v[58:59]
.LBB0_2812:
	v_readlane_b32 s0, v48, 15
	s_cmp_lt_i32 s0, 0
	s_cbranch_scc1 .LBB0_2781
	v_and_b32_e32 v48, 0xffff0000, v192
	v_lshlrev_b32_e32 v49, 16, v192
	v_and_b32_e32 v50, 0xffff0000, v193
	v_lshlrev_b32_e32 v51, 16, v193
	v_and_b32_e32 v58, 0xffff0000, v194
	v_lshlrev_b32_e32 v59, 16, v194
	v_and_b32_e32 v52, 0xffff0000, v195
	v_lshlrev_b32_e32 v53, 16, v195
	v_and_b32_e32 v60, 0xffff0000, v196
	v_lshlrev_b32_e32 v61, 16, v196
	v_and_b32_e32 v54, 0xffff0000, v197
	v_lshlrev_b32_e32 v55, 16, v197
	v_and_b32_e32 v62, 0xffff0000, v198
	v_lshlrev_b32_e32 v63, 16, v198
	v_and_b32_e32 v56, 0xffff0000, v199
	v_lshlrev_b32_e32 v57, 16, v199
	v_pk_add_f32 v[38:39], v[38:39], v[48:49]
	v_pk_add_f32 v[40:41], v[40:41], v[50:51]
	v_pk_add_f32 v[34:35], v[34:35], v[58:59]
	v_pk_add_f32 v[36:37], v[36:37], v[52:53]
	v_pk_add_f32 v[30:31], v[30:31], v[60:61]
	v_pk_add_f32 v[32:33], v[32:33], v[54:55]
	v_pk_add_f32 v[26:27], v[26:27], v[62:63]
	v_pk_add_f32 v[28:29], v[28:29], v[56:57]
	s_branch .LBB0_2781
